# v033 + topk: the four serialized (SV gather, wait, store, SU gather, wait, store) ladders per unit issue all 8 gathers first, one wait, then the stores
# speedup vs baseline: 1.0086x; 1.0014x over previous
; __device__ __forceinline__ float unmono(unsigned u) { return __uint_as_float((u & 0x80000000u) ? (u ^ 0x80000000u) : ~u); }
; __device__ __forceinline__ void topk_phase(LAS unsigned char* lds, const bf16_t* qp, const bf16_t* keys, const float* SU, const float* SV, int* sel_e, float* sel_g, float* sel_su, int G, int b) {
;     ...
;             for (int kk = 0; kk < 4; ++kk) {
;                 const unsigned W = fq == 0 ? ck[kk] : fq == 1 ? ck[4 + kk] : fq == 2 ? ck[8 + kk] : ck[12 + kk];
;                 const int k = fq * 4 + kk;
;                 const unsigned id = 255u - (W & 255u);
;                 const unsigned e1 = 127u - (wl[id >> 4] & 127u), e2 = 127u - (wl[16 + (id & 15u)] & 127u);
;                 const size_t o = ((size_t)tok * 8 + h) * 16 + k;
;                 const unsigned ex = e1 * 128u + e2;
;                 sel_e[o] = (int)ex; sel_g[o] = __expf(unmono(W & ~255u) - vmax) * einv * SV[ex]; sel_su[o] = SU[ex];
;             }
.LBB0_635:
	s_or_b64 exec, exec, s[0:1]
	v_not_b32_e32 v36, v40
	v_lshrrev_b32_e32 v36, 2, v36
	v_and_b32_e32 v36, 60, v36
	v_add_u32_e32 v36, v83, v36
	v_bitop3_b32 v37, v40, 15, v40 bitop3:0xc
	ds_read_b32 v36, v36
	v_lshl_add_u32 v37, v37, 2, v83
	ds_read_b32 v37, v37 offset:64
	v_or_b32_e32 v34, v34, v88
	v_lshlrev_b64 v[34:35], 2, v[34:35]
	s_waitcnt lgkmcnt(1)
	v_lshlrev_b32_e32 v36, 7, v36
	v_and_b32_e32 v36, 0x3f80, v36
	s_waitcnt lgkmcnt(0)
	v_and_b32_e32 v37, 0x7f, v37
	v_bitop3_b32 v38, v37, s61, v36 bitop3:0x36
	v_lshl_add_u64 v[36:37], s[46:47], 0, v[34:35]
	global_store_dword v[36:37], v38, off
	v_lshlrev_b32_e32 v38, 2, v38
	global_load_dword v188, v38, s[50:51]
	global_load_dword v189, v38, s[86:87]
	v_mul_f32_e32 v190, v43, v42
	v_mov_b64_e32 v[192:193], v[34:35]
	s_add_i32 s52, s52, 1
	s_mov_b64 s[0:1], 0
	s_waitcnt vmcnt(0)
	v_mul_f32_e32 v172, v172, v170
	v_lshl_add_u64 v[194:195], s[48:49], 0, v[174:175]
	global_store_dword v[194:195], v172, off
	v_lshl_add_u64 v[198:199], s[54:55], 0, v[174:175]
	global_store_dword v[198:199], v171, off
	v_mul_f32_e32 v178, v178, v176
	v_lshl_add_u64 v[196:197], s[48:49], 0, v[180:181]
	global_store_dword v[196:197], v178, off
	v_lshl_add_u64 v[200:201], s[54:55], 0, v[180:181]
	global_store_dword v[200:201], v177, off
	v_mul_f32_e32 v184, v184, v182
	v_lshl_add_u64 v[194:195], s[48:49], 0, v[186:187]
	global_store_dword v[194:195], v184, off
	v_lshl_add_u64 v[198:199], s[54:55], 0, v[186:187]
	global_store_dword v[198:199], v183, off
	v_mul_f32_e32 v190, v190, v188
	v_lshl_add_u64 v[196:197], s[48:49], 0, v[192:193]
	global_store_dword v[196:197], v190, off
	v_lshl_add_u64 v[200:201], s[54:55], 0, v[192:193]
	global_store_dword v[200:201], v189, off

; __device__ __forceinline__ float unmono(unsigned u) { return __uint_as_float((u & 0x80000000u) ? (u ^ 0x80000000u) : ~u); }
; __device__ __forceinline__ void topk_phase(LAS unsigned char* lds, const bf16_t* qp, const bf16_t* keys, const float* SU, const float* SV, int* sel_e, float* sel_g, float* sel_su, int G, int b) {
;     ...
;             const float vmax = unmono(ck[0] & ~255u);
;             float esum = 0.f;
; #pragma unroll
;             for (int k = 0; k < 16; ++k) esum += __expf(unmono(ck[k] & ~255u) - vmax);
;             const float einv = 1.0f / esum;
; #pragma unroll
;             for (int kk = 0; kk < 4; ++kk) {
;                 const unsigned W = fq == 0 ? ck[kk] : fq == 1 ? ck[4 + kk] : fq == 2 ? ck[8 + kk] : ck[12 + kk];
;                 const int k = fq * 4 + kk;
;                 const unsigned id = 255u - (W & 255u);
;                 const unsigned e1 = 127u - (wl[id >> 4] & 127u), e2 = 127u - (wl[16 + (id & 15u)] & 127u);
;                 const size_t o = ((size_t)tok * 8 + h) * 16 + k;
;                 const unsigned ex = e1 * 128u + e2;
;                 sel_e[o] = (int)ex; sel_g[o] = __expf(unmono(W & ~255u) - vmax) * einv * SV[ex]; sel_su[o] = SU[ex];
.LBB0_747:
	s_or_b64 exec, exec, s[0:1]
	v_min_u32_e32 v44, v44, v54
	v_min_u32_e32 v54, v48, v58
	v_min_u32_e32 v58, v59, v62
	v_min_u32_e32 v39, v39, v45
	v_min_u32_e32 v41, v41, v49
	v_cmp_lt_i32_e32 vcc, -1, v58
	v_min_u32_e32 v38, v38, v42
	v_min_u32_e32 v42, v40, v46
	v_min_u32_e32 v46, v50, v61
	v_max_u32_e32 v49, v39, v41
	v_min_u32_e32 v40, v39, v41
	v_max_u32_e32 v50, v44, v54
	v_min_u32_e32 v41, v44, v54
	v_cndmask_b32_e64 v44, v132, -1, vcc
	v_bitop3_b32 v44, v44, v58, s60 bitop3:0x78
	v_sub_f32_e32 v44, v44, v34
	v_mul_f32_e32 v44, 0x3fb8aa3b, v44
	v_cmp_lt_i32_e32 vcc, -1, v49
	v_min_u32_e32 v45, v47, v56
	v_min_u32_e32 v56, v55, v60
	v_min_u32_e32 v55, v52, v57
	v_exp_f32_e32 v57, v44
	v_cndmask_b32_e64 v44, v132, -1, vcc
	v_bitop3_b32 v44, v44, v49, s60 bitop3:0x78
	v_sub_f32_e32 v44, v44, v34
	v_mul_f32_e32 v44, 0x3fb8aa3b, v44
	v_min_u32_e32 v59, v51, v53
	v_exp_f32_e32 v51, v44
	v_max_u32_e32 v48, v38, v42
	v_min_u32_e32 v39, v38, v42
	v_add_f32_e32 v42, 0, v64
	v_add_f32_e32 v42, v57, v42
	v_cmp_lt_i32_e32 vcc, -1, v40
	v_add_f32_e32 v44, v51, v42
	v_max_u32_e32 v47, v45, v46
	v_cndmask_b32_e64 v42, v132, -1, vcc
	v_bitop3_b32 v42, v42, v40, s60 bitop3:0x78
	v_sub_f32_e32 v42, v42, v34
	v_mul_f32_e32 v42, 0x3fb8aa3b, v42
	v_exp_f32_e32 v42, v42
	v_cmp_lt_i32_e32 vcc, -1, v56
	v_min_u32_e32 v38, v45, v46
	s_ashr_i32 s57, s56, 31
	v_add_f32_e32 v44, v42, v44
	v_add_f32_e32 v43, v43, v44
	v_cndmask_b32_e64 v44, v132, -1, vcc
	v_bitop3_b32 v44, v44, v56, s60 bitop3:0x78
	v_sub_f32_e32 v44, v44, v34
	v_mul_f32_e32 v44, 0x3fb8aa3b, v44
	v_cmp_lt_i32_e32 vcc, -1, v48
	v_exp_f32_e32 v60, v44
	s_nop 0
	v_cndmask_b32_e64 v44, v132, -1, vcc
	v_bitop3_b32 v44, v44, v48, s60 bitop3:0x78
	v_sub_f32_e32 v44, v44, v34
	v_mul_f32_e32 v44, 0x3fb8aa3b, v44
	v_cmp_lt_i32_e32 vcc, -1, v39
	v_exp_f32_e32 v52, v44
	v_add_f32_e32 v43, v60, v43
	v_cndmask_b32_e64 v44, v132, -1, vcc
	v_bitop3_b32 v44, v44, v39, s60 bitop3:0x78
	v_sub_f32_e32 v44, v44, v34
	v_mul_f32_e32 v44, 0x3fb8aa3b, v44
	v_exp_f32_e32 v44, v44
	v_add_f32_e32 v43, v52, v43
	v_cmp_lt_i32_e32 vcc, -1, v55
	v_add_f32_e32 v43, v44, v43
	v_add_f32_e32 v37, v37, v43
	v_cndmask_b32_e64 v43, v132, -1, vcc
	v_bitop3_b32 v43, v43, v55, s60 bitop3:0x78
	v_sub_f32_e32 v43, v43, v34
	v_mul_f32_e32 v43, 0x3fb8aa3b, v43
	v_cmp_lt_i32_e32 vcc, -1, v47
	v_exp_f32_e32 v61, v43
	s_nop 0
	v_cndmask_b32_e64 v43, v132, -1, vcc
	v_bitop3_b32 v43, v43, v47, s60 bitop3:0x78
	v_sub_f32_e32 v43, v43, v34
	v_mul_f32_e32 v43, 0x3fb8aa3b, v43
	v_cmp_lt_i32_e32 vcc, -1, v38
	v_exp_f32_e32 v53, v43
	v_add_f32_e32 v37, v61, v37
	v_cndmask_b32_e64 v43, v132, -1, vcc
	v_bitop3_b32 v43, v43, v38, s60 bitop3:0x78
	v_sub_f32_e32 v43, v43, v34
	v_mul_f32_e32 v43, 0x3fb8aa3b, v43
	v_exp_f32_e32 v45, v43
	v_add_f32_e32 v37, v53, v37
	v_cmp_lt_i32_e32 vcc, -1, v59
	v_add_f32_e32 v37, v45, v37
	v_add_f32_e32 v35, v35, v37
	v_cndmask_b32_e64 v37, v132, -1, vcc
	v_bitop3_b32 v37, v37, v59, s60 bitop3:0x78
	v_sub_f32_e32 v37, v37, v34
	v_mul_f32_e32 v37, 0x3fb8aa3b, v37
	v_cmp_lt_i32_e32 vcc, -1, v50
	v_exp_f32_e32 v62, v37
	s_nop 0
	v_cndmask_b32_e64 v37, v132, -1, vcc
	v_bitop3_b32 v37, v37, v50, s60 bitop3:0x78
	v_sub_f32_e32 v37, v37, v34
	v_mul_f32_e32 v37, 0x3fb8aa3b, v37
	v_cmp_lt_i32_e32 vcc, -1, v41
	v_exp_f32_e32 v54, v37
	v_add_f32_e32 v35, v62, v35
	v_cndmask_b32_e64 v37, v132, -1, vcc
	v_bitop3_b32 v37, v37, v41, s60 bitop3:0x78
	v_sub_f32_e32 v34, v37, v34
	v_mul_f32_e32 v34, 0x3fb8aa3b, v34
	v_exp_f32_e32 v46, v34
	v_add_f32_e32 v35, v54, v35
	v_add_f32_e32 v34, v46, v35
	v_div_scale_f32 v35, s[0:1], v34, v34, 1.0
	v_rcp_f32_e32 v37, v35
	s_nop 0
	v_fma_f32 v43, -v35, v37, 1.0
	v_fmac_f32_e32 v37, v43, v37
	v_div_scale_f32 v43, vcc, 1.0, v34, 1.0
	v_mul_f32_e32 v64, v43, v37
	v_fma_f32 v65, -v35, v64, v43
	v_fmac_f32_e32 v64, v65, v37
	v_fma_f32 v35, -v35, v64, v43
	v_div_fmas_f32 v35, v35, v37, v64
	v_not_b32_e32 v37, v36
	v_lshrrev_b32_e32 v37, 2, v37
	v_and_b32_e32 v37, 60, v37
	v_bitop3_b32 v36, v36, 15, v36 bitop3:0xc
	v_add_u32_e32 v37, v83, v37
	v_lshl_add_u32 v36, v36, 2, v83
	ds_read_b32 v64, v37
	ds_read_b32 v36, v36 offset:64
	v_div_fixup_f32 v43, v35, v34, 1.0
	v_lshlrev_b64 v[34:35], 7, v[94:95]
	v_lshl_add_u64 v[34:35], s[56:57], 4, v[34:35]
	v_mov_b32_e32 v37, v35
	s_waitcnt lgkmcnt(0)
	v_and_b32_e32 v65, 0x7f, v36
	v_or_b32_e32 v36, v34, v82
	v_lshlrev_b32_e32 v64, 7, v64
	v_and_b32_e32 v64, 0x3f80, v64
	v_lshlrev_b64 v[36:37], 2, v[36:37]
	v_bitop3_b32 v66, v65, s61, v64 bitop3:0x36
	v_lshl_add_u64 v[64:65], s[46:47], 0, v[36:37]
	global_store_dword v[64:65], v66, off
	v_lshlrev_b32_e32 v66, 2, v66
	global_load_dword v170, v66, s[50:51]
	global_load_dword v171, v66, s[86:87]
	v_mul_f32_e32 v172, v43, v63
	v_mov_b64_e32 v[174:175], v[36:37]
	s_and_saveexec_b64 s[0:1], s[42:43]
	s_cbranch_execz .LBB0_755
	v_cmp_lt_i32_e32 vcc, 1, v1
	s_and_saveexec_b64 s[4:5], vcc
	s_xor_b64 s[4:5], exec, s[4:5]
	s_cbranch_execz .LBB0_752
	v_cmp_ne_u32_e32 vcc, 2, v1
	s_and_saveexec_b64 s[6:7], vcc
	v_mov_b32_e32 v55, v59
	v_mov_b32_e32 v61, v62
	s_or_b64 exec, exec, s[6:7]

; __device__ __forceinline__ float unmono(unsigned u) { return __uint_as_float((u & 0x80000000u) ? (u ^ 0x80000000u) : ~u); }
; __device__ __forceinline__ void topk_phase(LAS unsigned char* lds, const bf16_t* qp, const bf16_t* keys, const float* SU, const float* SV, int* sel_e, float* sel_g, float* sel_su, int G, int b) {
;     ...
;             for (int kk = 0; kk < 4; ++kk) {
;                 const unsigned W = fq == 0 ? ck[kk] : fq == 1 ? ck[4 + kk] : fq == 2 ? ck[8 + kk] : ck[12 + kk];
;                 const int k = fq * 4 + kk;
;                 const unsigned id = 255u - (W & 255u);
;                 const unsigned e1 = 127u - (wl[id >> 4] & 127u), e2 = 127u - (wl[16 + (id & 15u)] & 127u);
;                 const size_t o = ((size_t)tok * 8 + h) * 16 + k;
;                 const unsigned ex = e1 * 128u + e2;
;                 sel_e[o] = (int)ex; sel_g[o] = __expf(unmono(W & ~255u) - vmax) * einv * SV[ex]; sel_su[o] = SU[ex];
.LBB0_755:
	s_or_b64 exec, exec, s[0:1]
	v_not_b32_e32 v36, v58
	v_lshrrev_b32_e32 v36, 2, v36
	v_and_b32_e32 v36, 60, v36
	v_add_u32_e32 v36, v83, v36
	ds_read_b32 v55, v36
	v_bitop3_b32 v36, v58, 15, v58 bitop3:0xc
	v_lshl_add_u32 v36, v36, 2, v83
	ds_read_b32 v36, v36 offset:64
	v_mov_b32_e32 v37, v35
	s_waitcnt lgkmcnt(1)
	v_lshlrev_b32_e32 v55, 7, v55
	v_and_b32_e32 v55, 0x3f80, v55
	s_waitcnt lgkmcnt(0)
	v_and_b32_e32 v56, 0x7f, v36
	v_or_b32_e32 v36, v34, v84
	v_lshlrev_b64 v[36:37], 2, v[36:37]
	v_bitop3_b32 v55, v56, s61, v55 bitop3:0x36
	v_lshl_add_u64 v[58:59], s[46:47], 0, v[36:37]
	global_store_dword v[58:59], v55, off
	v_lshlrev_b32_e32 v55, 2, v55
	global_load_dword v176, v55, s[50:51]
	global_load_dword v177, v55, s[86:87]
	v_mul_f32_e32 v178, v43, v57
	v_mov_b64_e32 v[180:181], v[36:37]
	s_and_saveexec_b64 s[0:1], s[42:43]
	s_cbranch_execz .LBB0_763
	v_cmp_lt_i32_e32 vcc, 1, v1
	s_and_saveexec_b64 s[4:5], vcc
	s_xor_b64 s[4:5], exec, s[4:5]
	s_cbranch_execz .LBB0_760
	v_cmp_ne_u32_e32 vcc, 2, v1
	s_and_saveexec_b64 s[6:7], vcc
	v_mov_b32_e32 v47, v50
	v_mov_b32_e32 v53, v54
	s_or_b64 exec, exec, s[6:7]

; __device__ __forceinline__ float unmono(unsigned u) { return __uint_as_float((u & 0x80000000u) ? (u ^ 0x80000000u) : ~u); }
; __device__ __forceinline__ void topk_phase(LAS unsigned char* lds, const bf16_t* qp, const bf16_t* keys, const float* SU, const float* SV, int* sel_e, float* sel_g, float* sel_su, int G, int b) {
;     ...
;             for (int kk = 0; kk < 4; ++kk) {
;                 const unsigned W = fq == 0 ? ck[kk] : fq == 1 ? ck[4 + kk] : fq == 2 ? ck[8 + kk] : ck[12 + kk];
;                 const int k = fq * 4 + kk;
;                 const unsigned id = 255u - (W & 255u);
;                 const unsigned e1 = 127u - (wl[id >> 4] & 127u), e2 = 127u - (wl[16 + (id & 15u)] & 127u);
;                 const size_t o = ((size_t)tok * 8 + h) * 16 + k;
;                 const unsigned ex = e1 * 128u + e2;
;                 sel_e[o] = (int)ex; sel_g[o] = __expf(unmono(W & ~255u) - vmax) * einv * SV[ex]; sel_su[o] = SU[ex];
.LBB0_763:
	s_or_b64 exec, exec, s[0:1]
	v_not_b32_e32 v36, v49
	v_lshrrev_b32_e32 v36, 2, v36
	v_and_b32_e32 v36, 60, v36
	v_add_u32_e32 v36, v83, v36
	ds_read_b32 v47, v36
	v_bitop3_b32 v36, v49, 15, v49 bitop3:0xc
	v_lshl_add_u32 v36, v36, 2, v83
	ds_read_b32 v36, v36 offset:64
	v_mov_b32_e32 v37, v35
	s_waitcnt lgkmcnt(1)
	v_lshlrev_b32_e32 v47, 7, v47
	v_and_b32_e32 v47, 0x3f80, v47
	s_waitcnt lgkmcnt(0)
	v_and_b32_e32 v48, 0x7f, v36
	v_or_b32_e32 v36, v34, v86
	v_lshlrev_b64 v[36:37], 2, v[36:37]
	v_bitop3_b32 v47, v48, s61, v47 bitop3:0x36
	v_lshl_add_u64 v[48:49], s[46:47], 0, v[36:37]
	global_store_dword v[48:49], v47, off
	v_lshlrev_b32_e32 v47, 2, v47
	global_load_dword v182, v47, s[50:51]
	global_load_dword v183, v47, s[86:87]
	v_mul_f32_e32 v184, v43, v51
	v_mov_b64_e32 v[186:187], v[36:37]
	s_and_saveexec_b64 s[0:1], s[42:43]
	s_cbranch_execz .LBB0_635
	v_cmp_lt_i32_e32 vcc, 1, v1
	s_and_saveexec_b64 s[4:5], vcc
	s_xor_b64 s[4:5], exec, s[4:5]
	s_cbranch_execz .LBB0_768
	v_cmp_ne_u32_e32 vcc, 2, v1
	s_and_saveexec_b64 s[6:7], vcc
	v_mov_b32_e32 v38, v41
	v_mov_b32_e32 v45, v46
	s_or_b64 exec, exec, s[6:7]
